# adds: attention row-max/row-sum chains lose their self-max canonicalisations and the leading add with zero (5 VALU ops per tile per wave)
# baseline (speedup 1.0000x reference)
.LBB0_787:
	s_mov_b32 s54, s0
	s_add_i32 s55, s28, -3
	s_lshl_b32 s21, s0, 14
	v_add_u32_e32 v180, s21, v191
	v_add_u32_e32 v84, v180, v190
	ds_read_b128 v[80:83], v84 offset:50176
	ds_read_b128 v[84:87], v84 offset:58368
	v_add_u32_e32 v195, v180, v188
	ds_read_b128 v[196:199], v195 offset:50176
	ds_read_b128 v[200:203], v195 offset:58368
	v_add_u32_e32 v195, v180, v187
	s_waitcnt lgkmcnt(3)
	v_mfma_f32_32x32x16_bf16 v[96:111], v[80:83], v[122:125], 0
	v_add_u32_e32 v180, v180, v186
	v_exp_f32_e32 v204, v72
	v_exp_f32_e32 v205, v73
	v_exp_f32_e32 v206, v74
	v_exp_f32_e32 v207, v75
	v_exp_f32_e32 v208, v76
	v_exp_f32_e32 v209, v77
	s_waitcnt lgkmcnt(2)
	v_mfma_f32_32x32x16_bf16 v[80:95], v[84:87], v[122:125], 0
	v_exp_f32_e32 v210, v78
	v_exp_f32_e32 v79, v79
	s_waitcnt lgkmcnt(1)
	v_mfma_f32_32x32x16_bf16 v[96:111], v[196:199], v[126:129], v[96:111]
	s_waitcnt lgkmcnt(0)
	v_mfma_f32_32x32x16_bf16 v[80:95], v[200:203], v[126:129], v[80:95]
	ds_read_b128 v[196:199], v195 offset:50176
	ds_read_b128 v[200:203], v195 offset:58368
	s_waitcnt lgkmcnt(1)
	v_mfma_f32_32x32x16_bf16 v[96:111], v[196:199], v[118:121], v[96:111]
	s_waitcnt lgkmcnt(0)
	v_mfma_f32_32x32x16_bf16 v[80:95], v[200:203], v[118:121], v[80:95]
	ds_read_b128 v[196:199], v180 offset:50176
	ds_read_b128 v[200:203], v180 offset:58368
	v_exp_f32_e32 v180, v64
	v_add_f32_e32 v64, v161, v159
	v_add_f32_e32 v64, v157, v64
	v_add_f32_e32 v64, v160, v64
	v_add_f32_e32 v64, v155, v64
	v_add_f32_e32 v64, v158, v64
	v_add_f32_e32 v64, v154, v64
	v_add_f32_e32 v64, v156, v64
	v_add_f32_e32 v64, v151, v64
	v_add_f32_e32 v64, v153, v64
	v_add_f32_e32 v64, v149, v64
	v_add_f32_e32 v64, v152, v64
	v_add_f32_e32 v64, v147, v64
	s_waitcnt lgkmcnt(1)
	v_mfma_f32_32x32x16_bf16 v[96:111], v[196:199], v[114:117], v[96:111]
	v_exp_f32_e32 v197, v65
	v_add_f32_e32 v64, v150, v64
	v_exp_f32_e32 v198, v66
	v_add_f32_e32 v64, v146, v64
	v_exp_f32_e32 v199, v67
	v_add_f32_e32 v64, v148, v64
	v_add_f32_e32 v64, v180, v64
	s_waitcnt lgkmcnt(0)
	v_mfma_f32_32x32x16_bf16 v[80:95], v[200:203], v[114:117], v[80:95]
	v_exp_f32_e32 v200, v68
	v_exp_f32_e32 v201, v69
	v_add_f32_e32 v64, v197, v64
	v_exp_f32_e32 v202, v70
	v_add_f32_e32 v64, v198, v64
	v_exp_f32_e32 v203, v71
	v_add_f32_e32 v64, v199, v64
	v_add_f32_e32 v64, v200, v64
	v_add_f32_e32 v64, v201, v64
	v_add_f32_e32 v64, v202, v64
	v_add_f32_e32 v64, v203, v64
	v_add_f32_e32 v64, v204, v64
	v_add_f32_e32 v64, v205, v64
	v_add_f32_e32 v64, v206, v64
	v_add_f32_e32 v64, v207, v64
	v_add_f32_e32 v64, v208, v64
	v_add_f32_e32 v64, v209, v64
	v_add_f32_e32 v64, v210, v64
	v_add_f32_e32 v195, v79, v64
	v_mov_b32_e32 v196, v195
	v_cvt_pk_bf16_f32 v64, v159, v161
	v_cvt_pk_bf16_f32 v65, v157, v160
	v_cvt_pk_bf16_f32 v66, v155, v158
	s_nop 1
	v_permlane32_swap_b32_e32 v195, v196
	v_cvt_pk_bf16_f32 v67, v154, v156
	v_permlane32_swap_b32_e32 v64, v66
	v_cvt_pk_bf16_f32 v68, v151, v153
	v_cvt_pk_bf16_f32 v69, v149, v152
	v_cvt_pk_bf16_f32 v70, v147, v150
	v_cvt_pk_bf16_f32 v71, v146, v148
	v_cvt_pk_bf16_f32 v72, v180, v197
	v_cvt_pk_bf16_f32 v73, v198, v199
	v_cvt_pk_bf16_f32 v74, v200, v201
	v_cvt_pk_bf16_f32 v75, v202, v203
	v_cvt_pk_bf16_f32 v76, v204, v205
	v_cvt_pk_bf16_f32 v77, v206, v207
	v_cvt_pk_bf16_f32 v78, v208, v209
	v_cvt_pk_bf16_f32 v79, v210, v79
	v_permlane32_swap_b32_e32 v65, v67
	v_permlane32_swap_b32_e32 v68, v70
	v_permlane32_swap_b32_e32 v69, v71
	v_permlane32_swap_b32_e32 v72, v74
	v_permlane32_swap_b32_e32 v73, v75
	v_permlane32_swap_b32_e32 v76, v78
	v_permlane32_swap_b32_e32 v77, v79
	s_cmp_lt_u32 s55, 30
	s_cselect_b32 s0, 0, 0xffffffe0
	s_cselect_b32 s1, s18, s16
	s_add_i32 s0, s0, s28
	s_lshl_b32 s0, s0, 6
	s_add_i32 s0, s0, s1
	s_sub_i32 s0, s0, 64
	s_mul_i32 s64, s0, 0x1800
	s_add_u32 s66, s8, s96
	s_addc_u32 s67, s9, 0
	s_add_u32 s66, s66, s64
	s_addc_u32 s67, s67, 0
	s_add_u32 s68, s66, 0x30000
	s_addc_u32 s69, s67, 0
	s_add_u32 s70, s6, s96
	s_addc_u32 s71, s7, 0
	s_add_u32 s70, s70, s64
	s_addc_u32 s71, s71, 0
	s_add_u32 s72, s70, 0x30000
	s_addc_u32 s73, s71, 0
	global_load_dwordx4 v[146:149], v241, s[66:67]
	global_load_dwordx4 v[150:153], v241, s[68:69]
	global_load_dwordx4 v[154:157], v241, s[70:71]
	global_load_dwordx4 v[158:161], v241, s[72:73]
	s_lshl_b32 s20, s29, 14
	v_add_u32_e32 v180, s20, v194
	ds_read_b64_tr_b16 v[198:199], v180 offset:0
	ds_read_b64_tr_b16 v[200:201], v180 offset:0x800
	ds_read_b64_tr_b16 v[202:203], v180 offset:0x1000
	ds_read_b64_tr_b16 v[204:205], v180 offset:0x1800
	ds_read_b64_tr_b16 v[206:207], v180 offset:0x2000
	ds_read_b64_tr_b16 v[208:209], v180 offset:0x2800
	ds_read_b64_tr_b16 v[222:223], v180 offset:0x3000
	ds_read_b64_tr_b16 v[224:225], v180 offset:0x3800
	s_waitcnt lgkmcnt(0)
	s_nop 0
	v_mfma_f32_32x32x16_bf16 v[0:15], v[64:67], v[198:201], v[0:15]
	ds_read_b64_tr_b16 v[198:199], v180 offset:0x200
	ds_read_b64_tr_b16 v[200:201], v180 offset:0xa00
	v_mfma_f32_32x32x16_bf16 v[0:15], v[68:71], v[202:205], v[0:15]
	ds_read_b64_tr_b16 v[202:203], v180 offset:0x1200
	ds_read_b64_tr_b16 v[204:205], v180 offset:0x1a00
	v_mfma_f32_32x32x16_bf16 v[0:15], v[72:75], v[206:209], v[0:15]
	ds_read_b64_tr_b16 v[206:207], v180 offset:0x2200
	ds_read_b64_tr_b16 v[208:209], v180 offset:0x2a00
	v_mfma_f32_32x32x16_bf16 v[0:15], v[76:79], v[222:225], v[0:15]
	ds_read_b64_tr_b16 v[222:223], v180 offset:0x3200
	ds_read_b64_tr_b16 v[224:225], v180 offset:0x3a00
	s_waitcnt lgkmcnt(0)
	v_mfma_f32_32x32x16_bf16 v[48:63], v[64:67], v[198:201], v[48:63]
	ds_read_b64_tr_b16 v[198:199], v180 offset:0x400
	ds_read_b64_tr_b16 v[200:201], v180 offset:0xc00
	v_mfma_f32_32x32x16_bf16 v[48:63], v[68:71], v[202:205], v[48:63]
	ds_read_b64_tr_b16 v[202:203], v180 offset:0x1400
	ds_read_b64_tr_b16 v[204:205], v180 offset:0x1c00
	v_mfma_f32_32x32x16_bf16 v[48:63], v[72:75], v[206:209], v[48:63]
	ds_read_b64_tr_b16 v[206:207], v180 offset:0x2400
	ds_read_b64_tr_b16 v[208:209], v180 offset:0x2c00
	v_mfma_f32_32x32x16_bf16 v[48:63], v[76:79], v[222:225], v[48:63]
	ds_read_b64_tr_b16 v[222:223], v180 offset:0x3400
	ds_read_b64_tr_b16 v[224:225], v180 offset:0x3c00
	s_waitcnt lgkmcnt(0)
	v_mfma_f32_32x32x16_bf16 v[32:47], v[64:67], v[198:201], v[32:47]
	ds_read_b64_tr_b16 v[198:199], v180 offset:0x600
	ds_read_b64_tr_b16 v[200:201], v180 offset:0xe00
	v_mfma_f32_32x32x16_bf16 v[32:47], v[68:71], v[202:205], v[32:47]
	ds_read_b64_tr_b16 v[202:203], v180 offset:0x1600
	ds_read_b64_tr_b16 v[204:205], v180 offset:0x1e00
	v_mfma_f32_32x32x16_bf16 v[32:47], v[72:75], v[206:209], v[32:47]
	ds_read_b64_tr_b16 v[206:207], v180 offset:0x2600
	ds_read_b64_tr_b16 v[208:209], v180 offset:0x2e00
	v_mfma_f32_32x32x16_bf16 v[32:47], v[76:79], v[222:225], v[32:47]
	ds_read_b64_tr_b16 v[222:223], v180 offset:0x3600
	ds_read_b64_tr_b16 v[224:225], v180 offset:0x3e00
	s_waitcnt lgkmcnt(0)
	v_mfma_f32_32x32x16_bf16 v[16:31], v[64:67], v[198:201], v[16:31]
	v_max_f32_e32 v64, v96, v97
	v_max3_f32 v64, v64, v98, v99
	v_max3_f32 v64, v64, v100, v101
	v_max3_f32 v64, v64, v102, v103
	v_max3_f32 v64, v64, v104, v105
	v_mfma_f32_32x32x16_bf16 v[16:31], v[68:71], v[202:205], v[16:31]
	v_max3_f32 v64, v64, v106, v107
	v_max3_f32 v64, v64, v108, v109
	v_max3_f32 v64, v64, v110, v111
	v_max3_f32 v64, v64, v80, v81
	v_max3_f32 v64, v64, v82, v83
	v_max3_f32 v64, v64, v84, v85
	v_max3_f32 v64, v64, v86, v87
	v_mfma_f32_32x32x16_bf16 v[16:31], v[72:75], v[206:209], v[16:31]
	v_max3_f32 v64, v64, v88, v89
	v_max3_f32 v64, v64, v90, v91
	v_max3_f32 v64, v64, v92, v93
	v_max3_f32 v64, v64, v94, v95
	v_mov_b32_e32 v65, v64
	s_nop 1
	v_permlane32_swap_b32_e32 v64, v65
	v_mfma_f32_32x32x16_bf16 v[16:31], v[76:79], v[222:225], v[16:31]
	v_max_f32_e32 v64, v64, v65
	v_cmp_eq_f32_e32 vcc, 0, v164
	v_cmp_ge_f32_e64 s[40:41], s75, v64
	s_and_b64 s[0:1], vcc, s[40:41]
	s_cmp_eq_u64 s[0:1], exec
	v_mov_b32_e32 v198, 1.0
	s_cbranch_scc0 .LBB0_801

.LBB0_792:
	v_exp_f32_e32 v197, v96
	v_exp_f32_e32 v208, v97
	v_exp_f32_e32 v209, v98
	v_exp_f32_e32 v210, v99
	v_exp_f32_e32 v211, v100
	v_exp_f32_e32 v220, v101
	v_exp_f32_e32 v221, v102
	v_exp_f32_e32 v222, v103
	v_exp_f32_e32 v223, v104
	v_exp_f32_e32 v224, v105
	v_exp_f32_e32 v225, v106
	v_exp_f32_e32 v226, v107
	v_exp_f32_e32 v227, v108
	v_exp_f32_e32 v228, v109
	v_exp_f32_e32 v229, v110
	v_exp_f32_e32 v230, v111
	s_waitcnt lgkmcnt(0)
	s_barrier
	v_add_u32_e32 v199, s22, v189
	v_add_u32_e32 v68, v199, v190
	ds_read_b128 v[64:67], v68 offset:50176
	ds_read_b128 v[68:71], v68 offset:58368
	v_add_u32_e32 v204, v199, v188
	ds_read_b128 v[200:203], v204 offset:50176
	ds_read_b128 v[204:207], v204 offset:58368
	v_exp_f32_e32 v231, v87
	s_waitcnt lgkmcnt(3)
	v_mfma_f32_32x32x16_bf16 v[96:111], v[64:67], v[122:125], 0
	v_exp_f32_e32 v232, v88
	v_exp_f32_e32 v233, v89
	v_exp_f32_e32 v234, v90
	v_exp_f32_e32 v235, v91
	v_exp_f32_e32 v236, v92
	v_exp_f32_e32 v237, v93
	v_exp_f32_e32 v238, v94
	s_waitcnt lgkmcnt(2)
	v_mfma_f32_32x32x16_bf16 v[64:79], v[68:71], v[122:125], 0
	v_exp_f32_e32 v95, v95
	s_waitcnt lgkmcnt(1)
	v_mfma_f32_32x32x16_bf16 v[96:111], v[200:203], v[126:129], v[96:111]
	s_waitcnt lgkmcnt(0)
	v_mfma_f32_32x32x16_bf16 v[64:79], v[204:207], v[126:129], v[64:79]
	v_add_u32_e32 v204, v199, v187
	ds_read_b128 v[200:203], v204 offset:50176
	ds_read_b128 v[204:207], v204 offset:58368
	v_add_u32_e32 v199, v199, v186
	s_waitcnt lgkmcnt(1)
	v_mfma_f32_32x32x16_bf16 v[96:111], v[200:203], v[118:121], v[96:111]
	s_waitcnt lgkmcnt(0)
	v_mfma_f32_32x32x16_bf16 v[64:79], v[204:207], v[118:121], v[64:79]
	ds_read_b128 v[200:203], v199 offset:50176
	ds_read_b128 v[204:207], v199 offset:58368
	s_waitcnt lgkmcnt(1)
	v_mfma_f32_32x32x16_bf16 v[96:111], v[200:203], v[114:117], v[96:111]
	v_exp_f32_e32 v201, v80
	v_add_f32_e32 v80, v208, v197
	v_add_f32_e32 v80, v209, v80
	v_add_f32_e32 v80, v210, v80
	v_add_f32_e32 v80, v211, v80
	v_add_f32_e32 v80, v220, v80
	v_add_f32_e32 v80, v221, v80
	v_add_f32_e32 v80, v222, v80
	v_add_f32_e32 v80, v223, v80
	v_add_f32_e32 v80, v224, v80
	v_add_f32_e32 v80, v225, v80
	v_add_f32_e32 v80, v226, v80
	v_add_f32_e32 v80, v227, v80
	v_exp_f32_e32 v202, v81
	v_add_f32_e32 v80, v228, v80
	v_exp_f32_e32 v203, v82
	v_add_f32_e32 v80, v229, v80
	s_waitcnt lgkmcnt(0)
	v_mfma_f32_32x32x16_bf16 v[64:79], v[204:207], v[114:117], v[64:79]
	v_exp_f32_e32 v204, v83
	v_add_f32_e32 v80, v230, v80
	v_exp_f32_e32 v205, v84
	v_add_f32_e32 v80, v201, v80
	v_exp_f32_e32 v206, v85
	v_add_f32_e32 v80, v202, v80
	v_exp_f32_e32 v207, v86
	v_add_f32_e32 v80, v203, v80
	v_add_f32_e32 v80, v204, v80
	v_add_f32_e32 v80, v205, v80
	v_add_f32_e32 v80, v206, v80
	v_add_f32_e32 v80, v207, v80
	v_add_f32_e32 v80, v231, v80
	v_add_f32_e32 v80, v232, v80
	v_add_f32_e32 v80, v233, v80
	v_add_f32_e32 v80, v234, v80
	v_add_f32_e32 v80, v235, v80
	v_add_f32_e32 v80, v236, v80
	v_add_f32_e32 v80, v237, v80
	v_add_f32_e32 v80, v238, v80
	v_add_f32_e32 v199, v95, v80
	v_mov_b32_e32 v200, v199
	v_cvt_pk_bf16_f32 v80, v197, v208
	v_cvt_pk_bf16_f32 v81, v209, v210
	v_cvt_pk_bf16_f32 v82, v211, v220
	v_cvt_pk_bf16_f32 v83, v221, v222
	v_cvt_pk_bf16_f32 v84, v223, v224
	v_cvt_pk_bf16_f32 v85, v225, v226
	v_cvt_pk_bf16_f32 v86, v227, v228
	v_cvt_pk_bf16_f32 v87, v229, v230
	v_cvt_pk_bf16_f32 v88, v201, v202
	v_cvt_pk_bf16_f32 v89, v203, v204
	v_cvt_pk_bf16_f32 v90, v205, v206
	v_cvt_pk_bf16_f32 v91, v207, v231
	v_cvt_pk_bf16_f32 v92, v232, v233
	v_cvt_pk_bf16_f32 v93, v234, v235
	v_cvt_pk_bf16_f32 v94, v236, v237
	v_cvt_pk_bf16_f32 v95, v238, v95
	s_nop 1
	v_permlane32_swap_b32_e32 v199, v200
	v_permlane32_swap_b32_e32 v80, v82
	v_permlane32_swap_b32_e32 v81, v83
	v_permlane32_swap_b32_e32 v84, v86
	v_permlane32_swap_b32_e32 v85, v87
	v_permlane32_swap_b32_e32 v88, v90
	v_permlane32_swap_b32_e32 v89, v91
	v_permlane32_swap_b32_e32 v92, v94
	v_permlane32_swap_b32_e32 v93, v95
	s_cmp_gt_u32 s55, 32
	s_cbranch_scc1 .LBB0_794
	s_cmp_lt_u32 s55, 29
	s_cselect_b32 s0, 0, 0xffffffe0
	s_cselect_b32 s1, s18, s16
	s_add_i32 s0, s0, s28
	s_lshl_b32 s0, s0, 6
	s_add_i32 s0, s0, s1
	s_mul_i32 s64, s0, 0x1800
	s_add_u32 s66, s8, s96
	s_addc_u32 s67, s9, 0
	s_add_u32 s66, s66, s64
	s_addc_u32 s67, s67, 0
	s_add_u32 s68, s66, 0x30000
	s_addc_u32 s69, s67, 0
	s_add_u32 s70, s6, s96
	s_addc_u32 s71, s7, 0
	s_add_u32 s70, s70, s64
	s_addc_u32 s71, s71, 0
	s_add_u32 s72, s70, 0x30000
	s_addc_u32 s73, s71, 0
	global_load_dwordx4 v[130:133], v241, s[66:67]
	global_load_dwordx4 v[134:137], v241, s[68:69]
	global_load_dwordx4 v[138:141], v241, s[70:71]
	global_load_dwordx4 v[142:145], v241, s[72:73]
.LBB0_794:
	v_add_u32_e32 v197, s21, v194
	ds_read_b64_tr_b16 v[202:203], v197 offset:0
	ds_read_b64_tr_b16 v[204:205], v197 offset:0x800
	ds_read_b64_tr_b16 v[206:207], v197 offset:0x1000
	ds_read_b64_tr_b16 v[208:209], v197 offset:0x1800
	ds_read_b64_tr_b16 v[222:223], v197 offset:0x2000
	ds_read_b64_tr_b16 v[224:225], v197 offset:0x2800
	ds_read_b64_tr_b16 v[226:227], v197 offset:0x3000
	ds_read_b64_tr_b16 v[228:229], v197 offset:0x3800
	s_waitcnt lgkmcnt(0)
	s_nop 0
	v_mfma_f32_32x32x16_bf16 v[0:15], v[80:83], v[202:205], v[0:15]
	ds_read_b64_tr_b16 v[202:203], v197 offset:0x200
	ds_read_b64_tr_b16 v[204:205], v197 offset:0xa00
	v_mfma_f32_32x32x16_bf16 v[0:15], v[84:87], v[206:209], v[0:15]
	ds_read_b64_tr_b16 v[206:207], v197 offset:0x1200
	ds_read_b64_tr_b16 v[208:209], v197 offset:0x1a00
	v_mfma_f32_32x32x16_bf16 v[0:15], v[88:91], v[222:225], v[0:15]
	ds_read_b64_tr_b16 v[222:223], v197 offset:0x2200
	ds_read_b64_tr_b16 v[224:225], v197 offset:0x2a00
	v_mfma_f32_32x32x16_bf16 v[0:15], v[92:95], v[226:229], v[0:15]
	ds_read_b64_tr_b16 v[226:227], v197 offset:0x3200
	ds_read_b64_tr_b16 v[228:229], v197 offset:0x3a00
	s_waitcnt lgkmcnt(0)
	v_mfma_f32_32x32x16_bf16 v[48:63], v[80:83], v[202:205], v[48:63]
	ds_read_b64_tr_b16 v[202:203], v197 offset:0x400
	ds_read_b64_tr_b16 v[204:205], v197 offset:0xc00
	v_mfma_f32_32x32x16_bf16 v[48:63], v[84:87], v[206:209], v[48:63]
	ds_read_b64_tr_b16 v[206:207], v197 offset:0x1400
	ds_read_b64_tr_b16 v[208:209], v197 offset:0x1c00
	v_mfma_f32_32x32x16_bf16 v[48:63], v[88:91], v[222:225], v[48:63]
	ds_read_b64_tr_b16 v[222:223], v197 offset:0x2400
	ds_read_b64_tr_b16 v[224:225], v197 offset:0x2c00
	v_mfma_f32_32x32x16_bf16 v[48:63], v[92:95], v[226:229], v[48:63]
	ds_read_b64_tr_b16 v[226:227], v197 offset:0x3400
	ds_read_b64_tr_b16 v[228:229], v197 offset:0x3c00
	s_waitcnt lgkmcnt(0)
	v_mfma_f32_32x32x16_bf16 v[32:47], v[80:83], v[202:205], v[32:47]
	ds_read_b64_tr_b16 v[202:203], v197 offset:0x600
	ds_read_b64_tr_b16 v[204:205], v197 offset:0xe00
	v_mfma_f32_32x32x16_bf16 v[32:47], v[84:87], v[206:209], v[32:47]
	ds_read_b64_tr_b16 v[206:207], v197 offset:0x1600
	ds_read_b64_tr_b16 v[208:209], v197 offset:0x1e00
	v_mfma_f32_32x32x16_bf16 v[32:47], v[88:91], v[222:225], v[32:47]
	ds_read_b64_tr_b16 v[222:223], v197 offset:0x2600
	ds_read_b64_tr_b16 v[224:225], v197 offset:0x2e00
	v_mfma_f32_32x32x16_bf16 v[32:47], v[92:95], v[226:229], v[32:47]
	ds_read_b64_tr_b16 v[226:227], v197 offset:0x3600
	ds_read_b64_tr_b16 v[228:229], v197 offset:0x3e00
	s_waitcnt lgkmcnt(0)
	v_mfma_f32_32x32x16_bf16 v[16:31], v[80:83], v[202:205], v[16:31]
	v_max_f32_e32 v80, v96, v97
	v_max3_f32 v80, v80, v98, v99
	v_max3_f32 v80, v80, v100, v101
	v_max3_f32 v80, v80, v102, v103
	v_max3_f32 v80, v80, v104, v105
	v_mfma_f32_32x32x16_bf16 v[16:31], v[84:87], v[206:209], v[16:31]
	v_max3_f32 v80, v80, v106, v107
	v_max3_f32 v80, v80, v108, v109
	v_max3_f32 v80, v80, v110, v111
	v_max3_f32 v80, v80, v64, v65
	v_max3_f32 v80, v80, v66, v67
	v_max3_f32 v80, v80, v68, v69
	v_max3_f32 v80, v80, v70, v71
	v_mfma_f32_32x32x16_bf16 v[16:31], v[88:91], v[222:225], v[16:31]
	v_max3_f32 v80, v80, v72, v73
	v_max3_f32 v80, v80, v74, v75
	v_max3_f32 v80, v80, v76, v77
	v_max3_f32 v80, v80, v78, v79
	v_mov_b32_e32 v81, v80
	s_nop 1
	v_permlane32_swap_b32_e32 v80, v81
	v_mfma_f32_32x32x16_bf16 v[16:31], v[92:95], v[226:229], v[16:31]
	v_max_f32_e32 v80, v80, v81
	v_cmp_eq_f32_e32 vcc, 0, v164
	v_cmp_ge_f32_e64 s[40:41], s75, v80
	s_and_b64 s[0:1], vcc, s[40:41]
	s_cmp_eq_u64 s[0:1], exec
	v_mov_b32_e32 v197, 1.0
	s_cbranch_scc0 .LBB0_802
